# P5 epilogue: second-half residual loads issued together (one wait fewer) + 9 of 16 store pairs widened to dwordx4
# baseline (speedup 1.0000x reference)
.LBB0_490:
	v_bfe_u32 v254, v178, 4, 1
	v_mov_b32_e32 v255, 0
	v_mul_u32_u24_e32 v254, 24, v254
	s_ashr_i32 s6, s68, 31
	s_lshr_b32 s6, s6, 21
	s_add_i32 s6, s68, s6
	s_lshr_b32 s6, s6, 11
	s_mulk_i32 s6, 0x3000
	s_ashr_i32 s7, s6, 31
	s_lshl_b64 s[6:7], s[6:7], 2
	s_add_u32 s26, s92, s6
	s_addc_u32 s27, s93, s7
	s_ashr_i32 s25, s24, 31
	s_lshl_b64 s[6:7], s[24:25], 2
	s_add_u32 s6, s26, s6
	s_addc_u32 s7, s27, s7
	s_add_u32 s6, s6, s57
	v_add_u32_e32 v146, s68, v201
	s_addc_u32 s7, s7, 0
	v_mov_b32_e32 v197, v183
	v_ashrrev_i32_e32 v147, 31, v146
	v_lshl_add_u64 v[128:129], s[6:7], 0, v[196:197]
	v_lshl_add_u64 v[144:145], v[190:191], 0, s[24:25]
	v_lshlrev_b64 v[148:149], 11, v[146:147]
	v_lshl_add_u64 v[130:131], v[128:129], 0, s[20:21]
	v_add_co_u32_e32 v128, vcc, s49, v128
	v_lshl_add_u64 v[198:199], v[144:145], 0, v[148:149]
	s_nop 0
	v_addc_co_u32_e32 v129, vcc, 0, v129, vcc
	v_lshl_add_u64 v[232:233], v[198:199], 2, s[8:9]
	v_add_co_u32_e32 v210, vcc, s58, v232
	global_load_dwordx4 v[136:139], v[130:131], off offset:64
	global_load_dwordx4 v[132:135], v[130:131], off offset:512
	global_load_dwordx4 v[140:143], v[128:129], off
	s_nop 0
	global_load_dwordx4 v[128:131], v[130:131], off offset:576
	v_addc_co_u32_e32 v211, vcc, 0, v233, vcc
	global_load_dwordx4 v[148:151], v[232:233], off
	global_load_dwordx4 v[152:155], v[232:233], off offset:64
	global_load_dwordx4 v[156:159], v[232:233], off offset:512
	global_load_dwordx4 v[160:163], v[232:233], off offset:576
	global_load_dwordx4 v[164:167], v[210:211], off
	global_load_dwordx4 v[168:171], v[210:211], off offset:64
	global_load_dwordx4 v[172:175], v[210:211], off offset:512
	s_nop 0
	global_load_dwordx4 v[210:213], v[210:211], off offset:576
	v_add_co_u32_e32 v228, vcc, s59, v232
	v_lshl_add_u64 v[198:199], v[198:199], 1, s[16:17]
	s_nop 0
	v_addc_co_u32_e32 v229, vcc, 0, v233, vcc
	global_load_dwordx4 v[214:217], v[228:229], off
	global_load_dwordx4 v[220:223], v[228:229], off offset:64
	global_load_dwordx4 v[224:227], v[228:229], off offset:512
	s_nop 0
	global_load_dwordx4 v[228:231], v[228:229], off offset:576
	v_add_co_u32_e32 v244, vcc, s60, v232
	s_mov_b32 s25, s64
	s_nop 0
	v_addc_co_u32_e32 v245, vcc, 0, v233, vcc
	global_load_dwordx4 v[232:235], v[244:245], off
	global_load_dwordx4 v[236:239], v[244:245], off offset:64
	global_load_dwordx4 v[240:243], v[244:245], off offset:512
	s_nop 0
	global_load_dwordx4 v[244:247], v[244:245], off offset:576
	v_add_co_u32_e32 v248, vcc, s48, v198
	s_mov_b64 s[26:27], s[22:23]
	s_nop 0
	v_addc_co_u32_e32 v249, vcc, 0, v199, vcc
	s_mov_b32 s68, s65
	s_mov_b32 s24, s63
	s_waitcnt vmcnt(0)
	v_pk_fma_f32 v[126:127], v[126:127], v[142:143], v[150:151]
	v_pk_fma_f32 v[124:125], v[124:125], v[140:141], v[148:149]
	v_pk_fma_f32 v[122:123], v[122:123], v[138:139], v[154:155]
	v_pk_fma_f32 v[120:121], v[120:121], v[136:137], v[152:153]
	v_pk_fma_f32 v[94:95], v[94:95], v[130:131], v[212:213]
	v_pk_fma_f32 v[92:93], v[92:93], v[128:129], v[210:211]
	v_pk_fma_f32 v[110:111], v[110:111], v[134:135], v[158:159]
	v_pk_fma_f32 v[108:109], v[108:109], v[132:133], v[156:157]
	v_pk_fma_f32 v[106:107], v[106:107], v[130:131], v[162:163]
	v_pk_fma_f32 v[104:105], v[104:105], v[128:129], v[160:161]
	v_pk_fma_f32 v[118:119], v[118:119], v[142:143], v[166:167]
	v_pk_fma_f32 v[116:117], v[116:117], v[140:141], v[164:165]
	v_pk_fma_f32 v[114:115], v[114:115], v[138:139], v[170:171]
	v_pk_fma_f32 v[112:113], v[112:113], v[136:137], v[168:169]
	v_pk_fma_f32 v[102:103], v[102:103], v[134:135], v[174:175]
	v_pk_fma_f32 v[100:101], v[100:101], v[132:133], v[172:173]
	v_cvt_pk_bf16_f32 v124, v124, v125
	v_cvt_pk_bf16_f32 v125, v126, v127
	v_cvt_pk_bf16_f32 v92, v92, v93
	v_cvt_pk_bf16_f32 v93, v94, v95
	v_cvt_pk_bf16_f32 v120, v120, v121
	v_cvt_pk_bf16_f32 v121, v122, v123
	v_cvt_pk_bf16_f32 v108, v108, v109
	v_cvt_pk_bf16_f32 v109, v110, v111
	v_cvt_pk_bf16_f32 v104, v104, v105
	v_cvt_pk_bf16_f32 v105, v106, v107
	v_cvt_pk_bf16_f32 v106, v116, v117
	v_cvt_pk_bf16_f32 v107, v118, v119
	v_cvt_pk_bf16_f32 v110, v112, v113
	v_cvt_pk_bf16_f32 v111, v114, v115
	v_cvt_pk_bf16_f32 v100, v100, v101
	v_cvt_pk_bf16_f32 v101, v102, v103
	v_mov_b32_e32 v126, v120
	v_mov_b32_e32 v127, v121
	v_lshl_add_u64 v[252:253], v[198:199], 0, v[254:255]
	s_nop 0
	v_permlane16_swap_b32_e32 v124, v126
	v_permlane16_swap_b32_e32 v125, v127
	global_store_dwordx4 v[252:253], v[124:127], off
	s_nop 1
	v_mov_b32_e32 v102, v108
	v_mov_b32_e32 v103, v109
	v_lshl_add_u64 v[252:253], v[198:199], 0, v[254:255]
	s_nop 0
	v_permlane16_swap_b32_e32 v102, v104
	v_permlane16_swap_b32_e32 v103, v105
	global_store_dwordx4 v[252:253], v[102:105], off offset:256
	s_nop 1
	v_mov_b32_e32 v108, v110
	v_mov_b32_e32 v109, v111
	v_lshl_add_u64 v[252:253], v[248:249], 0, v[254:255]
	s_nop 0
	v_permlane16_swap_b32_e32 v106, v108
	v_permlane16_swap_b32_e32 v107, v109
	global_store_dwordx4 v[252:253], v[106:109], off
	s_nop 1
	v_mov_b32_e32 v102, v92
	v_mov_b32_e32 v103, v93
	v_lshl_add_u64 v[252:253], v[248:249], 0, v[254:255]
	s_nop 0
	v_permlane16_swap_b32_e32 v100, v102
	v_permlane16_swap_b32_e32 v101, v103
	global_store_dwordx4 v[252:253], v[100:103], off offset:256
	s_nop 1
	v_pk_fma_f32 v[92:93], v[98:99], v[142:143], v[216:217]
	v_pk_fma_f32 v[94:95], v[96:97], v[140:141], v[214:215]
	v_pk_fma_f32 v[78:79], v[78:79], v[130:131], v[230:231]
	v_cvt_pk_bf16_f32 v94, v94, v95
	v_cvt_pk_bf16_f32 v95, v92, v93
	v_add_co_u32_e32 v92, vcc, s58, v198
	v_pk_fma_f32 v[76:77], v[76:77], v[128:129], v[228:229]
	s_nop 0
	v_addc_co_u32_e32 v93, vcc, 0, v199, vcc
	v_cvt_pk_bf16_f32 v76, v76, v77
	v_cvt_pk_bf16_f32 v77, v78, v79
	global_store_dwordx2 v[92:93], v[76:77], off offset:288
	v_pk_fma_f32 v[76:77], v[86:87], v[142:143], v[234:235]
	v_pk_fma_f32 v[78:79], v[84:85], v[140:141], v[232:233]
	v_pk_fma_f32 v[66:67], v[66:67], v[130:131], v[246:247]
	v_cvt_pk_bf16_f32 v78, v78, v79
	v_cvt_pk_bf16_f32 v79, v76, v77
	v_add_co_u32_e32 v76, vcc, s61, v198
	v_pk_fma_f32 v[64:65], v[64:65], v[128:129], v[244:245]
	s_nop 0
	v_addc_co_u32_e32 v77, vcc, 0, v199, vcc
	v_cvt_pk_bf16_f32 v64, v64, v65
	v_cvt_pk_bf16_f32 v65, v66, v67
	global_store_dwordx2 v[76:77], v[64:65], off offset:288
	v_add_u32_e32 v64, 0x80, v146
	v_ashrrev_i32_e32 v65, 31, v64
	v_pk_fma_f32 v[90:91], v[90:91], v[138:139], v[222:223]
	v_pk_fma_f32 v[88:89], v[88:89], v[136:137], v[220:221]
	v_pk_fma_f32 v[82:83], v[82:83], v[134:135], v[226:227]
	v_pk_fma_f32 v[80:81], v[80:81], v[132:133], v[224:225]
	v_pk_fma_f32 v[74:75], v[74:75], v[138:139], v[238:239]
	v_pk_fma_f32 v[72:73], v[72:73], v[136:137], v[236:237]
	v_pk_fma_f32 v[70:71], v[70:71], v[134:135], v[242:243]
	v_pk_fma_f32 v[68:69], v[68:69], v[132:133], v[240:241]
	v_lshlrev_b64 v[64:65], 11, v[64:65]
	v_cvt_pk_bf16_f32 v88, v88, v89
	v_cvt_pk_bf16_f32 v89, v90, v91
	v_cvt_pk_bf16_f32 v80, v80, v81
	v_cvt_pk_bf16_f32 v81, v82, v83
	v_cvt_pk_bf16_f32 v72, v72, v73
	v_cvt_pk_bf16_f32 v73, v74, v75
	v_cvt_pk_bf16_f32 v68, v68, v69
	v_cvt_pk_bf16_f32 v69, v70, v71
	v_lshl_add_u64 v[144:145], v[64:65], 0, v[144:145]
	v_mov_b32_e32 v96, v88
	v_mov_b32_e32 v97, v89
	v_lshl_add_u64 v[252:253], v[92:93], 0, v[254:255]
	s_nop 0
	v_permlane16_swap_b32_e32 v94, v96
	v_permlane16_swap_b32_e32 v95, v97
	global_store_dwordx4 v[252:253], v[94:97], off
	s_nop 1
	global_store_dwordx2 v[92:93], v[80:81], off offset:256
	v_mov_b32_e32 v80, v72
	v_mov_b32_e32 v81, v73
	v_lshl_add_u64 v[252:253], v[76:77], 0, v[254:255]
	s_nop 0
	v_permlane16_swap_b32_e32 v78, v80
	v_permlane16_swap_b32_e32 v79, v81
	global_store_dwordx4 v[252:253], v[78:81], off
	s_nop 1
	global_store_dwordx2 v[76:77], v[68:69], off offset:256
	v_lshl_add_u64 v[112:113], v[144:145], 2, s[8:9]
	global_load_dwordx4 v[64:67], v[112:113], off
	global_load_dwordx4 v[68:71], v[112:113], off offset:64
	global_load_dwordx4 v[72:75], v[112:113], off offset:512
	global_load_dwordx4 v[76:79], v[112:113], off offset:576
	v_add_co_u32_e32 v92, vcc, s58, v112
	s_nop 1
	v_addc_co_u32_e32 v93, vcc, 0, v113, vcc
	global_load_dwordx4 v[80:83], v[92:93], off
	global_load_dwordx4 v[84:87], v[92:93], off offset:64
	global_load_dwordx4 v[88:91], v[92:93], off offset:512
	s_nop 0
	global_load_dwordx4 v[92:95], v[92:93], off offset:576
	v_add_co_u32_e32 v108, vcc, s59, v112
	s_nop 1
	v_addc_co_u32_e32 v109, vcc, 0, v113, vcc
	global_load_dwordx4 v[96:99], v[108:109], off
	global_load_dwordx4 v[100:103], v[108:109], off offset:64
	global_load_dwordx4 v[104:107], v[108:109], off offset:512
	s_nop 0
	global_load_dwordx4 v[108:111], v[108:109], off offset:576
	v_add_co_u32_e32 v124, vcc, s60, v112
	s_nop 1
	v_addc_co_u32_e32 v125, vcc, 0, v113, vcc
	global_load_dwordx4 v[112:115], v[124:125], off
	global_load_dwordx4 v[116:119], v[124:125], off offset:64
	global_load_dwordx4 v[120:123], v[124:125], off offset:512
	s_nop 0
	global_load_dwordx4 v[124:127], v[124:125], off offset:576
	s_waitcnt vmcnt(12)
	v_pk_fma_f32 v[62:63], v[62:63], v[142:143], v[66:67]
	v_pk_fma_f32 v[60:61], v[60:61], v[140:141], v[64:65]
	v_pk_fma_f32 v[46:47], v[46:47], v[130:131], v[78:79]
	v_pk_fma_f32 v[44:45], v[44:45], v[128:129], v[76:77]
	v_cvt_pk_bf16_f32 v60, v60, v61
	v_cvt_pk_bf16_f32 v61, v62, v63
	v_lshl_add_u64 v[62:63], v[144:145], 1, s[16:17]
	v_cvt_pk_bf16_f32 v44, v44, v45
	v_cvt_pk_bf16_f32 v45, v46, v47
	global_store_dwordx2 v[62:63], v[44:45], off offset:288
	v_pk_fma_f32 v[58:59], v[58:59], v[138:139], v[70:71]
	v_pk_fma_f32 v[56:57], v[56:57], v[136:137], v[68:69]
	v_pk_fma_f32 v[54:55], v[54:55], v[134:135], v[74:75]
	v_pk_fma_f32 v[52:53], v[52:53], v[132:133], v[72:73]
	v_cvt_pk_bf16_f32 v56, v56, v57
	v_cvt_pk_bf16_f32 v57, v58, v59
	v_cvt_pk_bf16_f32 v52, v52, v53
	v_cvt_pk_bf16_f32 v53, v54, v55
	global_store_dwordx2 v[62:63], v[60:61], off
	global_store_dwordx2 v[62:63], v[56:57], off offset:32
	global_store_dwordx2 v[62:63], v[52:53], off offset:256
	s_waitcnt vmcnt(0)
	v_pk_fma_f32 v[44:45], v[50:51], v[142:143], v[82:83]
	v_pk_fma_f32 v[46:47], v[48:49], v[140:141], v[80:81]
	v_pk_fma_f32 v[42:43], v[42:43], v[138:139], v[86:87]
	v_cvt_pk_bf16_f32 v46, v46, v47
	v_cvt_pk_bf16_f32 v47, v44, v45
	v_add_co_u32_e32 v44, vcc, s48, v62
	v_pk_fma_f32 v[30:31], v[30:31], v[130:131], v[94:95]
	v_pk_fma_f32 v[28:29], v[28:29], v[128:129], v[92:93]
	v_addc_co_u32_e32 v45, vcc, 0, v63, vcc
	v_cvt_pk_bf16_f32 v28, v28, v29
	v_cvt_pk_bf16_f32 v29, v30, v31
	global_store_dwordx2 v[44:45], v[28:29], off offset:288
	v_pk_fma_f32 v[28:29], v[34:35], v[142:143], v[98:99]
	v_pk_fma_f32 v[30:31], v[32:33], v[140:141], v[96:97]
	v_pk_fma_f32 v[14:15], v[14:15], v[130:131], v[110:111]
	v_cvt_pk_bf16_f32 v30, v30, v31
	v_cvt_pk_bf16_f32 v31, v28, v29
	v_add_co_u32_e32 v28, vcc, s58, v62
	v_pk_fma_f32 v[12:13], v[12:13], v[128:129], v[108:109]
	s_nop 0
	v_addc_co_u32_e32 v29, vcc, 0, v63, vcc
	v_cvt_pk_bf16_f32 v12, v12, v13
	v_cvt_pk_bf16_f32 v13, v14, v15
	global_store_dwordx2 v[28:29], v[12:13], off offset:288
	v_pk_fma_f32 v[12:13], v[18:19], v[142:143], v[114:115]
	v_pk_fma_f32 v[14:15], v[16:17], v[140:141], v[112:113]
	v_pk_fma_f32 v[40:41], v[40:41], v[136:137], v[84:85]
	v_cvt_pk_bf16_f32 v14, v14, v15
	v_cvt_pk_bf16_f32 v15, v12, v13
	v_add_co_u32_e32 v12, vcc, s61, v62
	v_pk_fma_f32 v[38:39], v[38:39], v[134:135], v[90:91]
	v_pk_fma_f32 v[36:37], v[36:37], v[132:133], v[88:89]
	v_pk_fma_f32 v[26:27], v[26:27], v[138:139], v[102:103]
	v_pk_fma_f32 v[24:25], v[24:25], v[136:137], v[100:101]
	v_pk_fma_f32 v[22:23], v[22:23], v[134:135], v[106:107]
	v_pk_fma_f32 v[20:21], v[20:21], v[132:133], v[104:105]
	v_addc_co_u32_e32 v13, vcc, 0, v63, vcc
	v_pk_fma_f32 v[10:11], v[10:11], v[138:139], v[118:119]
	v_pk_fma_f32 v[8:9], v[8:9], v[136:137], v[116:117]
	v_pk_fma_f32 v[6:7], v[6:7], v[134:135], v[122:123]
	v_pk_fma_f32 v[4:5], v[4:5], v[132:133], v[120:121]
	v_pk_fma_f32 v[2:3], v[2:3], v[130:131], v[126:127]
	v_pk_fma_f32 v[0:1], v[0:1], v[128:129], v[124:125]
	v_cvt_pk_bf16_f32 v40, v40, v41
	v_cvt_pk_bf16_f32 v41, v42, v43
	v_cvt_pk_bf16_f32 v36, v36, v37
	v_cvt_pk_bf16_f32 v37, v38, v39
	v_cvt_pk_bf16_f32 v24, v24, v25
	v_cvt_pk_bf16_f32 v25, v26, v27
	v_cvt_pk_bf16_f32 v20, v20, v21
	v_cvt_pk_bf16_f32 v21, v22, v23
	v_cvt_pk_bf16_f32 v8, v8, v9
	v_cvt_pk_bf16_f32 v9, v10, v11
	v_cvt_pk_bf16_f32 v4, v4, v5
	v_cvt_pk_bf16_f32 v5, v6, v7
	v_cvt_pk_bf16_f32 v0, v0, v1
	v_cvt_pk_bf16_f32 v1, v2, v3
	s_and_b64 vcc, exec, s[2:3]
	global_store_dwordx2 v[44:45], v[46:47], off
	global_store_dwordx2 v[44:45], v[40:41], off offset:32
	global_store_dwordx2 v[44:45], v[36:37], off offset:256
	v_mov_b32_e32 v22, v30
	v_mov_b32_e32 v23, v31
	v_lshl_add_u64 v[252:253], v[28:29], 0, v[254:255]
	s_nop 0
	v_permlane16_swap_b32_e32 v22, v24
	v_permlane16_swap_b32_e32 v23, v25
	global_store_dwordx4 v[252:253], v[22:25], off
	s_nop 1
	global_store_dwordx2 v[28:29], v[20:21], off offset:256
	v_mov_b32_e32 v16, v8
	v_mov_b32_e32 v17, v9
	v_lshl_add_u64 v[252:253], v[12:13], 0, v[254:255]
	s_nop 0
	v_permlane16_swap_b32_e32 v14, v16
	v_permlane16_swap_b32_e32 v15, v17
	global_store_dwordx4 v[252:253], v[14:17], off
	s_nop 1
	v_mov_b32_e32 v6, v0
	v_mov_b32_e32 v7, v1
	v_lshl_add_u64 v[252:253], v[12:13], 0, v[254:255]
	s_nop 0
	v_permlane16_swap_b32_e32 v4, v6
	v_permlane16_swap_b32_e32 v5, v7
	global_store_dwordx4 v[252:253], v[4:7], off offset:256
	s_nop 1
	s_cbranch_vccnz .LBB0_504
